# N1 norm row loop: throw-away loads of the wave's next row issued after the current row's loads (cache warming), waits raised accordingly
# speedup vs baseline: 1.0029x; 1.0010x over previous
.LBB0_386:
	v_readlane_b32 s14, v255, 31
	v_readlane_b32 s15, v255, 32
	s_mov_b64 s[4:5], -1
	s_and_b64 vcc, exec, s[14:15]
	s_cbranch_vccz .LBB0_388
	v_readlane_b32 s40, v251, 5
	v_readlane_b32 s46, v251, 11
	v_readlane_b32 s47, v251, 12
	v_readlane_b32 s41, v251, 6
	v_readlane_b32 s42, v251, 7
	v_lshl_add_u64 v[50:51], s[46:47], 0, v[80:81]
	v_add_co_u32_e32 v50, vcc, 0x500000, v50
	v_readlane_b32 s43, v251, 8
	s_nop 0
	v_addc_co_u32_e32 v51, vcc, 0, v51, vcc
	global_load_dwordx2 v[52:53], v[50:51], off
	global_load_dwordx2 v[54:55], v[50:51], off offset:512
	global_load_dwordx2 v[56:57], v[50:51], off offset:1024
	global_load_dwordx2 v[92:93], v[50:51], off offset:1536
	v_lshl_add_u64 v[130:131], v[50:51], 0, v[72:73]
	global_load_dwordx2 v[132:133], v[130:131], off
	global_load_dwordx2 v[132:133], v[130:131], off offset:512
	global_load_dwordx2 v[132:133], v[130:131], off offset:1024
	global_load_dwordx2 v[132:133], v[130:131], off offset:1536
	v_readlane_b32 s44, v251, 9
	v_readlane_b32 s45, v251, 10
	s_mov_b64 s[4:5], 0
	s_waitcnt vmcnt(7)
	v_lshlrev_b32_e32 v62, 16, v52
	v_and_b32_e32 v63, 0xffff0000, v52
	v_lshlrev_b32_e32 v64, 16, v53
	v_and_b32_e32 v65, 0xffff0000, v53
	s_waitcnt vmcnt(6)
	v_lshlrev_b32_e32 v58, 16, v54
	v_and_b32_e32 v59, 0xffff0000, v54
	v_lshlrev_b32_e32 v60, 16, v55
	v_and_b32_e32 v61, 0xffff0000, v55
	s_waitcnt vmcnt(5)
	v_lshlrev_b32_e32 v54, 16, v56
	v_and_b32_e32 v55, 0xffff0000, v56
	v_lshlrev_b32_e32 v56, 16, v57
	v_and_b32_e32 v57, 0xffff0000, v57
	s_waitcnt vmcnt(4)
	v_lshlrev_b32_e32 v50, 16, v92
	v_and_b32_e32 v51, 0xffff0000, v92
	v_lshlrev_b32_e32 v52, 16, v93
	v_and_b32_e32 v53, 0xffff0000, v93
.LBB0_388:
	s_andn2_b64 vcc, exec, s[4:5]
	s_cbranch_vccnz .LBB0_390
	s_lshl_b64 s[4:5], s[8:9], 12
	v_readlane_b32 s40, v251, 28
	v_readlane_b32 s41, v251, 29
	s_add_u32 s3, s40, s4
	s_addc_u32 s4, s41, s5
	v_mov_b32_e32 v50, s4
	v_cndmask_b32_e64 v51, v50, v85, s[0:1]
	v_mov_b32_e32 v50, s3
	v_cndmask_b32_e64 v50, v50, v84, s[0:1]
	v_readfirstlane_b32 s1, v51
	v_readfirstlane_b32 s0, v50
	s_nop 4
	global_load_dwordx4 v[62:65], v1, s[0:1]
	global_load_dwordx4 v[58:61], v1, s[0:1] offset:1024
	global_load_dwordx4 v[54:57], v1, s[0:1] offset:2048
	global_load_dwordx4 v[50:53], v1, s[0:1] offset:3072
	global_load_dwordx4 v[132:135], v1, s[0:1]
	global_load_dwordx4 v[132:135], v1, s[0:1] offset:1024
	global_load_dwordx4 v[132:135], v1, s[0:1] offset:2048
	global_load_dwordx4 v[132:135], v1, s[0:1] offset:3072
	v_readlane_b32 s48, v251, 36
	v_readlane_b32 s49, v251, 37
	v_readlane_b32 s48, v255, 16
	v_readlane_b32 s49, v255, 17
	v_readlane_b32 s42, v251, 30
	v_readlane_b32 s43, v251, 31
	v_readlane_b32 s44, v251, 32
	v_readlane_b32 s45, v251, 33
	v_readlane_b32 s46, v251, 34
	v_readlane_b32 s47, v251, 35
	v_readlane_b32 s50, v251, 38
	v_readlane_b32 s51, v251, 39
	v_readlane_b32 s52, v251, 40
	v_readlane_b32 s53, v251, 41
	v_readlane_b32 s54, v251, 42
	v_readlane_b32 s55, v251, 43
.LBB0_390:
	s_waitcnt vmcnt(7)
	v_pk_mul_f32 v[96:97], v[64:65], v[64:65]
	v_pk_mul_f32 v[98:99], v[62:63], v[62:63]
	s_waitcnt vmcnt(6)
	v_pk_mul_f32 v[92:93], v[60:61], v[60:61]
	v_pk_mul_f32 v[94:95], v[58:59], v[58:59]
	v_pk_mov_b32 v[100:101], v[98:99], v[96:97] op_sel:[1,0]
	v_mov_b32_e32 v99, v97
	v_pk_add_f32 v[96:97], v[100:101], v[98:99]
	v_pk_mov_b32 v[98:99], v[94:95], v[92:93] op_sel:[1,0]
	v_mov_b32_e32 v95, v93
	v_pk_add_f32 v[92:93], v[98:99], v[94:95]
	v_pk_add_f32 v[96:97], v[96:97], v[96:97] op_sel_hi:[0,1]
	v_pk_add_f32 v[92:93], v[92:93], v[92:93] op_sel_hi:[0,1]
	s_waitcnt vmcnt(5)
	v_mul_f32_e32 v92, v54, v54
	v_pk_fma_f32 v[94:95], v[54:55], v[54:55], v[92:93] op_sel_hi:[1,1,0]
	v_mul_f32_e32 v92, v56, v56
	v_pk_fma_f32 v[98:99], v[56:57], v[56:57], v[92:93] op_sel_hi:[1,1,0]
	s_waitcnt vmcnt(4)
	v_mul_f32_e32 v94, v50, v50
	v_mul_f32_e32 v98, v51, v51
	v_mul_f32_e32 v96, v52, v52
	v_mul_f32_e32 v92, v53, v53
	v_pk_add_f32 v[94:95], v[94:95], v[98:99]
	v_pk_add_f32 v[92:93], v[96:97], v[92:93]
	s_mov_b32 s0, 0xf800000
	v_pk_add_f32 v[92:93], v[94:95], v[92:93]
	s_mov_b32 s3, 0x42fe0000
	v_add_f32_e32 v91, v92, v93
	ds_bpermute_b32 v92, v66, v91
	v_readlane_b32 s40, v251, 5
	v_readlane_b32 s46, v251, 11
	v_readlane_b32 s47, v251, 12
	v_readlane_b32 s41, v251, 6
	s_waitcnt lgkmcnt(0)
	v_add_f32_e32 v91, v91, v92
	ds_bpermute_b32 v92, v86, v91
	v_readlane_b32 s42, v251, 7
	v_readlane_b32 s43, v251, 8
	v_readlane_b32 s44, v251, 9
	v_readlane_b32 s45, v251, 10
	s_waitcnt lgkmcnt(0)
	v_add_f32_e32 v91, v91, v92
	ds_bpermute_b32 v92, v87, v91
	s_waitcnt lgkmcnt(0)
	v_add_f32_e32 v91, v91, v92
	ds_bpermute_b32 v92, v88, v91
	s_waitcnt lgkmcnt(0)
	v_add_f32_e32 v91, v91, v92
	ds_bpermute_b32 v92, v89, v91
	s_waitcnt lgkmcnt(0)
	v_add_f32_e32 v91, v91, v92
	ds_bpermute_b32 v92, v90, v91
	s_waitcnt lgkmcnt(0)
	v_add_f32_e32 v91, v91, v92
	v_fmamk_f32 v91, v91, 0x3a800000, v241
	v_mul_f32_e32 v92, 0x4f800000, v91
	v_cmp_gt_f32_e32 vcc, s0, v91
	s_nop 1
	v_cndmask_b32_e32 v91, v91, v92, vcc
	v_sqrt_f32_e32 v94, v91
	v_pk_add_f32 v[92:93], v[28:29], 1.0 op_sel_hi:[1,0]
	v_add_u32_e32 v95, -1, v94
	v_add_u32_e32 v96, 1, v94
	v_fma_f32 v97, -v95, v94, v91
	v_fma_f32 v98, -v96, v94, v91
	v_cmp_ge_f32_e64 s[0:1], 0, v97
	s_nop 1
	v_cndmask_b32_e64 v94, v94, v95, s[0:1]
	v_cmp_lt_f32_e64 s[0:1], 0, v98
	s_nop 1
	v_cndmask_b32_e64 v94, v94, v96, s[0:1]
	v_mul_f32_e32 v95, 0x37800000, v94
	v_cndmask_b32_e32 v94, v94, v95, vcc
	v_cmp_class_f32_e32 vcc, v91, v188
	s_nop 1
	v_cndmask_b32_e32 v91, v94, v91, vcc
	v_div_scale_f32 v96, s[0:1], v91, v91, 1.0
	v_rcp_f32_e32 v97, v96
	v_div_scale_f32 v98, vcc, 1.0, v91, 1.0
	v_pk_add_f32 v[94:95], v[26:27], 1.0 op_sel_hi:[1,0]
	v_fma_f32 v99, -v96, v97, 1.0
	v_fmac_f32_e32 v97, v99, v97
	v_mul_f32_e32 v99, v98, v97
	v_fma_f32 v100, -v96, v99, v98
	v_fmac_f32_e32 v99, v100, v97
	v_fma_f32 v96, -v96, v99, v98
	v_div_fmas_f32 v96, v96, v97, v99
	v_div_fixup_f32 v96, v96, v91, 1.0
	v_pk_mul_f32 v[64:65], v[64:65], v[96:97] op_sel_hi:[1,0]
	v_pk_mul_f32 v[62:63], v[62:63], v[96:97] op_sel_hi:[1,0]
	v_pk_mul_f32 v[64:65], v[16:17], v[64:65]
	v_pk_mul_f32 v[62:63], v[14:15], v[62:63]
	v_pk_mul_f32 v[60:61], v[60:61], v[96:97] op_sel_hi:[1,0]
	v_pk_mul_f32 v[58:59], v[58:59], v[96:97] op_sel_hi:[1,0]
	v_pk_fma_f32 v[64:65], v[92:93], v[64:65], v[20:21]
	v_pk_fma_f32 v[62:63], v[94:95], v[62:63], v[18:19]
	v_pk_mul_f32 v[58:59], v[10:11], v[58:59]
	v_pk_mul_f32 v[60:61], v[12:13], v[60:61]
	v_pk_add_f32 v[92:93], v[24:25], 1.0 op_sel_hi:[1,0]
	v_pk_add_f32 v[94:95], v[22:23], 1.0 op_sel_hi:[1,0]
	v_pk_mul_f32 v[56:57], v[56:57], v[96:97] op_sel_hi:[1,0]
	v_pk_mul_f32 v[54:55], v[54:55], v[96:97] op_sel_hi:[1,0]
	v_pk_fma_f32 v[60:61], v[92:93], v[60:61], v[32:33]
	v_pk_fma_f32 v[58:59], v[94:95], v[58:59], v[30:31]
	v_pk_mul_f32 v[54:55], v[6:7], v[54:55]
	v_pk_mul_f32 v[56:57], v[8:9], v[56:57]
	v_pk_add_f32 v[92:93], v[40:41], 1.0 op_sel_hi:[1,0]
	v_pk_add_f32 v[94:95], v[38:39], 1.0 op_sel_hi:[1,0]
	v_pk_mul_f32 v[52:53], v[52:53], v[96:97] op_sel_hi:[1,0]
	v_pk_mul_f32 v[50:51], v[50:51], v[96:97] op_sel_hi:[1,0]
	v_pk_fma_f32 v[56:57], v[92:93], v[56:57], v[44:45]
	v_pk_fma_f32 v[54:55], v[94:95], v[54:55], v[42:43]
	v_pk_mul_f32 v[50:51], v[2:3], v[50:51]
	v_pk_mul_f32 v[52:53], v[4:5], v[52:53]
	v_pk_add_f32 v[92:93], v[36:37], 1.0 op_sel_hi:[1,0]
	v_pk_add_f32 v[94:95], v[34:35], 1.0 op_sel_hi:[1,0]
	v_pk_fma_f32 v[52:53], v[92:93], v[52:53], v[48:49]
	v_pk_fma_f32 v[92:93], v[94:95], v[50:51], v[46:47]
	v_max_f32_e64 v50, |v62|, |v63|
	v_max_f32_e64 v51, |v64|, |v65|
	v_max3_f32 v50, v50, 0, v51
	v_max_f32_e64 v51, |v58|, |v59|
	v_max_f32_e64 v91, |v60|, |v61|
	v_max3_f32 v50, v50, v51, v91
	v_max_f32_e64 v51, |v54|, |v55|
	v_max_f32_e64 v91, |v56|, |v57|
	v_max3_f32 v50, v50, v51, v91
	v_max_f32_e64 v51, |v92|, |v93|
	v_max_f32_e64 v91, |v52|, |v53|
	v_max3_f32 v50, v50, v51, v91
	ds_bpermute_b32 v51, v66, v50
	s_waitcnt lgkmcnt(0)
	v_max_f32_e32 v51, v51, v51
	v_max_f32_e32 v50, v50, v51
	ds_bpermute_b32 v51, v86, v50
	s_waitcnt lgkmcnt(0)
	v_max_f32_e32 v51, v51, v51
	v_max_f32_e32 v50, v50, v51
	ds_bpermute_b32 v51, v87, v50
	s_waitcnt lgkmcnt(0)
	v_max_f32_e32 v51, v51, v51
	v_max_f32_e32 v50, v50, v51
	ds_bpermute_b32 v51, v88, v50
	s_waitcnt lgkmcnt(0)
	v_max_f32_e32 v51, v51, v51
	v_max_f32_e32 v50, v50, v51
	ds_bpermute_b32 v51, v89, v50
	s_waitcnt lgkmcnt(0)
	v_max_f32_e32 v51, v51, v51
	v_max_f32_e32 v50, v50, v51
	ds_bpermute_b32 v51, v90, v50
	s_waitcnt lgkmcnt(0)
	v_max_f32_e32 v51, v51, v51
	v_max_f32_e32 v50, v50, v51
	v_div_scale_f32 v51, s[0:1], v50, v50, s3
	v_rcp_f32_e32 v91, v51
	s_mov_b32 s0, 0x40c0c00
	s_mov_b32 s1, 0x8900000
	v_fma_f32 v94, -v51, v91, 1.0
	v_fmac_f32_e32 v91, v94, v91
	v_div_scale_f32 v94, vcc, s3, v50, s3
	v_mul_f32_e32 v95, v94, v91
	v_fma_f32 v96, -v51, v95, v94
	v_fmac_f32_e32 v95, v96, v91
	v_fma_f32 v51, -v51, v95, v94
	v_div_fmas_f32 v51, v51, v91, v95
	v_div_fixup_f32 v51, v51, v50, s3
	v_cmp_lt_f32_e32 vcc, 0, v50
	v_lshl_add_u64 v[94:95], s[46:47], 0, v[82:83]
	s_nop 0
	v_cndmask_b32_e32 v51, 0, v51, vcc
	v_mul_f32_e32 v63, v63, v51
	v_mul_f32_e32 v62, v62, v51
	v_rndne_f32_e32 v63, v63
	v_mul_f32_e32 v64, v64, v51
	v_mul_f32_e32 v65, v65, v51
	v_mul_f32_e32 v55, v55, v51
	v_rndne_f32_e32 v62, v62
	v_cvt_i32_f32_e32 v63, v63
	v_rndne_f32_e32 v64, v64
	v_rndne_f32_e32 v65, v65
	v_mul_f32_e32 v54, v54, v51
	v_rndne_f32_e32 v55, v55
	v_mul_f32_e32 v56, v56, v51
	v_mul_f32_e32 v57, v57, v51
	v_cvt_i32_f32_e32 v62, v62
	v_cvt_i32_f32_sdwa v64, v64 dst_sel:WORD_1 dst_unused:UNUSED_PAD src0_sel:DWORD
	v_cvt_i32_f32_e32 v65, v65
	v_rndne_f32_e32 v54, v54
	v_cvt_i32_f32_e32 v55, v55
	v_rndne_f32_e32 v56, v56
	v_rndne_f32_e32 v57, v57
	v_cvt_i32_f32_e32 v54, v54
	v_cvt_i32_f32_sdwa v56, v56 dst_sel:WORD_1 dst_unused:UNUSED_PAD src0_sel:DWORD
	v_cvt_i32_f32_e32 v57, v57
	v_lshlrev_b32_e32 v63, 8, v63
	v_and_b32_e32 v63, 0xff00, v63
	v_and_b32_e32 v64, 0xff0000, v64
	v_perm_b32 v62, v65, v62, s0
	v_lshlrev_b32_e32 v55, 8, v55
	v_or3_b32 v64, v62, v63, v64
	v_add_co_u32_e32 v62, vcc, s1, v94
	v_and_b32_e32 v55, 0xff00, v55
	v_and_b32_e32 v56, 0xff0000, v56
	v_perm_b32 v54, v57, v54, s0
	v_addc_co_u32_e32 v63, vcc, 0, v95, vcc
	v_mul_f32_e32 v59, v59, v51
	v_or3_b32 v54, v54, v55, v56
	v_mul_f32_e32 v55, v93, v51
	v_mul_f32_e32 v58, v58, v51
	v_rndne_f32_e32 v59, v59
	v_mul_f32_e32 v60, v60, v51
	v_mul_f32_e32 v61, v61, v51
	global_store_dword v[62:63], v54, off offset:512
	v_mul_f32_e32 v54, v92, v51
	v_rndne_f32_e32 v55, v55
	v_mul_f32_e32 v52, v52, v51
	v_mul_f32_e32 v51, v53, v51
	v_rndne_f32_e32 v58, v58
	v_cvt_i32_f32_e32 v59, v59
	v_rndne_f32_e32 v60, v60
	v_rndne_f32_e32 v61, v61
	v_rndne_f32_e32 v54, v54
	v_cvt_i32_f32_e32 v55, v55
	v_rndne_f32_e32 v52, v52
	v_rndne_f32_e32 v51, v51
	v_cvt_i32_f32_e32 v58, v58
	v_cvt_i32_f32_sdwa v60, v60 dst_sel:WORD_1 dst_unused:UNUSED_PAD src0_sel:DWORD
	v_cvt_i32_f32_e32 v61, v61
	v_cvt_i32_f32_e32 v54, v54
	v_cvt_i32_f32_sdwa v52, v52 dst_sel:WORD_1 dst_unused:UNUSED_PAD src0_sel:DWORD
	v_cvt_i32_f32_e32 v51, v51
	v_lshlrev_b32_e32 v59, 8, v59
	v_lshlrev_b32_e32 v53, 8, v55
	v_and_b32_e32 v59, 0xff00, v59
	v_and_b32_e32 v60, 0xff0000, v60
	v_perm_b32 v58, v61, v58, s0
	v_and_b32_e32 v53, 0xff00, v53
	v_and_b32_e32 v52, 0xff0000, v52
	v_perm_b32 v51, v51, v54, s0
	v_or3_b32 v58, v58, v59, v60
	v_or3_b32 v51, v51, v53, v52
	global_store_dword v[62:63], v64, off
	global_store_dword v[62:63], v58, off offset:256
	global_store_dword v[62:63], v51, off offset:768
	s_and_saveexec_b64 s[0:1], s[36:37]
	s_cbranch_execz .LBB0_383
	v_readlane_b32 s40, v251, 5
	v_readlane_b32 s46, v251, 11
	v_readlane_b32 s47, v251, 12
	v_mul_f32_e32 v52, 0x3c010204, v50
	v_readlane_b32 s41, v251, 6
	v_lshl_add_u64 v[50:51], s[46:47], 0, v[78:79]
	v_readlane_b32 s42, v251, 7
	v_readlane_b32 s43, v251, 8
	v_readlane_b32 s44, v251, 9
	v_readlane_b32 s45, v251, 10
	global_store_dword v[50:51], v52, off
	s_branch .LBB0_383
